# norm-loop DPP reductions + P1 prefetch fix + MoE counter loads issued together + scatter loop loads de-serialised
# speedup vs baseline: 1.0047x; 1.0047x over previous
.LBB0_1069:
	s_or_b64 exec, exec, s[6:7]
	v_readlane_b32 s8, v255, 19
	s_bitcmp1_b32 s45, 0
	v_readlane_b32 s9, v255, 20
	s_cselect_b64 s[4:5], -1, 0
	s_xor_b64 s[8:9], s[8:9], -1
	s_or_b64 s[4:5], s[8:9], s[4:5]
	v_writelane_b32 v255, s4, 23
	s_mov_b64 s[6:7], -1
	s_waitcnt lgkmcnt(0)
	v_writelane_b32 v255, s5, 24
	s_barrier
	v_readlane_b32 s4, v255, 21
	v_readlane_b32 s5, v255, 22
	s_andn2_b64 vcc, exec, s[4:5]
	s_cbranch_vccnz .LBB0_1363
	s_mov_b64 s[4:5], s[0:1]
	s_load_dwordx2 s[10:11], s[4:5], 0xd0
	s_lshl_b64 s[6:7], s[52:53], 2
	v_mbcnt_lo_u32_b32 v0, -1, 0
	v_mbcnt_hi_u32_b32 v0, -1, v0
	v_readlane_b32 s62, v254, 63
	v_add_u32_e32 v6, s67, v0
	s_waitcnt lgkmcnt(0)
	s_add_u32 s4, s10, s6
	v_writelane_b32 v255, s6, 21
	s_addc_u32 s5, s11, s7
	v_mov_b32_e32 v0, 0x10000
	global_load_dword v0, v0, s[4:5] sc1
	s_add_u32 s8, s4, 0x10000
	s_addc_u32 s9, s5, 0
	s_add_u32 s16, s10, 0x200000
	s_addc_u32 s17, s11, 0
	v_writelane_b32 v255, s7, 22
	global_load_dword v2, v1, s[8:9] offset:256 sc1
	global_load_dword v3, v1, s[8:9] offset:512 sc1
	global_load_dword v4, v1, s[8:9] offset:768 sc1
	global_load_dword v5, v1, s[8:9] offset:1024 sc1
	global_load_dword v7, v1, s[8:9] offset:1280 sc1
	global_load_dword v8, v1, s[8:9] offset:1536 sc1
	global_load_dword v9, v1, s[8:9] offset:1792 sc1
	v_readlane_b32 s63, v255, 0
	s_waitcnt vmcnt(7)
	v_readfirstlane_b32 s4, v0
	s_nop 0
	s_addk_i32 s4, 0xff
	s_and_b32 s6, s4, 0xffffff00
	s_waitcnt vmcnt(6)
	v_readfirstlane_b32 s4, v2
	s_nop 0
	s_addk_i32 s4, 0xff
	s_and_b32 s7, s4, 0xffffff00
	s_add_i32 s7, s7, s6
	s_waitcnt vmcnt(5)
	v_readfirstlane_b32 s4, v3
	s_nop 0
	s_addk_i32 s4, 0xff
	s_and_b32 s30, s4, 0xffffff00
	s_add_i32 s30, s30, s7
	s_waitcnt vmcnt(4)
	v_readfirstlane_b32 s4, v4
	s_nop 0
	s_addk_i32 s4, 0xff
	s_and_b32 s31, s4, 0xffffff00
	s_add_i32 s31, s31, s30
	s_waitcnt vmcnt(3)
	v_readfirstlane_b32 s4, v5
	s_nop 0
	s_addk_i32 s4, 0xff
	s_and_b32 s33, s4, 0xffffff00
	s_add_i32 s33, s33, s31
	s_waitcnt vmcnt(2)
	v_readfirstlane_b32 s4, v7
	s_nop 0
	s_addk_i32 s4, 0xff
	s_and_b32 s34, s4, 0xffffff00
	s_add_i32 s34, s34, s33
	s_waitcnt vmcnt(1)
	v_readfirstlane_b32 s4, v8
	s_nop 0
	s_addk_i32 s4, 0xff
	s_and_b32 s35, s4, 0xffffff00
	v_readlane_b32 s4, v253, 3
	v_readlane_b32 s5, v253, 4
	s_andn2_b64 vcc, exec, s[4:5]
	v_readlane_b32 s4, v254, 61
	s_add_i32 s35, s35, s34
	s_mov_b32 s52, s4
	v_readlane_b32 s5, v254, 62
	s_cbranch_vccnz .LBB0_1081
	v_not_b32_e32 v7, v6
	s_mov_b32 s4, s2
	s_branch .LBB0_1073

.LBB0_1085:
	s_add_i32 s20, s42, s40
	s_add_i32 s24, s65, s40
	s_mul_i32 s22, s46, 24
	s_add_i32 s22, s22, s40
	s_ashr_i32 s10, s40, 1
	s_ashr_i32 s11, s10, 31
	s_lshl_b64 s[10:11], s[10:11], 2
	s_add_u32 s10, s36, s10
	s_addc_u32 s11, s37, s11
	global_load_dword v40, v1, s[10:11]
	global_load_dwordx2 v[32:33], v1, s[18:19]
	s_cmp_lt_i32 s20, 0x10000
	s_cselect_b32 s44, 1, 0
	s_cbranch_scc0 .Lsc_ld1
	s_ashr_i32 s10, s20, 1
	s_ashr_i32 s11, s10, 31
	s_lshl_b64 s[10:11], s[10:11], 2
	s_add_u32 s10, s36, s10
	s_addc_u32 s11, s37, s11
	global_load_dword v41, v1, s[10:11]
	s_ashr_i32 s11, s20, 31
	s_mov_b32 s10, s20
	s_lshl_b64 s[10:11], s[10:11], 3
	s_add_u32 s10, s4, s10
	s_addc_u32 s11, s5, s11
	global_load_dwordx2 v[34:35], v1, s[10:11]
.Lsc_ld1:
	s_cmp_lt_i32 s24, 0x10000
	s_cselect_b32 s45, 1, 0
	s_cbranch_scc0 .Lsc_ld2
	s_ashr_i32 s10, s24, 1
	s_ashr_i32 s11, s10, 31
	s_lshl_b64 s[10:11], s[10:11], 2
	s_add_u32 s10, s36, s10
	s_addc_u32 s11, s37, s11
	global_load_dword v42, v1, s[10:11]
	s_ashr_i32 s11, s24, 31
	s_mov_b32 s10, s24
	s_lshl_b64 s[10:11], s[10:11], 3
	s_add_u32 s10, s4, s10
	s_addc_u32 s11, s5, s11
	global_load_dwordx2 v[36:37], v1, s[10:11]
.Lsc_ld2:
	s_cmp_lt_i32 s22, 0x10000
	s_cselect_b32 s48, 1, 0
	s_cbranch_scc0 .Lsc_ld3
	s_ashr_i32 s10, s22, 1
	s_ashr_i32 s11, s10, 31
	s_lshl_b64 s[10:11], s[10:11], 2
	s_add_u32 s10, s36, s10
	s_addc_u32 s11, s37, s11
	global_load_dword v43, v1, s[10:11]
	s_ashr_i32 s11, s22, 31
	s_mov_b32 s10, s22
	s_lshl_b64 s[10:11], s[10:11], 3
	s_add_u32 s10, s4, s10
	s_addc_u32 s11, s5, s11
	global_load_dwordx2 v[38:39], v1, s[10:11]
.Lsc_ld3:
	s_waitcnt vmcnt(0)
	v_readfirstlane_b32 s41, v32
	s_nop 0
	s_ashr_i32 s26, s41, 24
	s_cmp_eq_u32 s26, 1
	s_cselect_b32 s27, s6, 0
	s_cmp_eq_u32 s26, 2
	s_cselect_b32 s27, s7, s27
	s_cmp_eq_u32 s26, 3
	s_cselect_b32 s27, s30, s27
	s_cmp_eq_u32 s26, 4
	s_cselect_b32 s27, s31, s27
	s_cmp_eq_u32 s26, 5
	s_cselect_b32 s27, s33, s27
	s_cmp_eq_u32 s26, 6
	s_cselect_b32 s27, s34, s27
	s_cmp_eq_u32 s26, 7
	s_cselect_b32 s26, s35, s27
	s_and_b32 s27, s41, 0xffffff
	s_add_i32 s12, s26, s27
	v_mov_b32_e32 v32, s40
	s_ashr_i32 s10, s40, 1
	s_ashr_i32 s11, s10, 31
	s_lshl_b64 s[10:11], s[10:11], 10
	v_lshl_add_u64 v[2:3], v[20:21], 0, s[10:11]
	global_load_dwordx4 v[44:47], v[2:3], off
	s_cmp_eq_u32 s44, 0
	s_cbranch_scc1 .Lsc_rw1
	v_readfirstlane_b32 s41, v34
	s_nop 0
	s_ashr_i32 s26, s41, 24
	s_cmp_eq_u32 s26, 1
	s_cselect_b32 s27, s6, 0
	s_cmp_eq_u32 s26, 2
	s_cselect_b32 s27, s7, s27
	s_cmp_eq_u32 s26, 3
	s_cselect_b32 s27, s30, s27
	s_cmp_eq_u32 s26, 4
	s_cselect_b32 s27, s31, s27
	s_cmp_eq_u32 s26, 5
	s_cselect_b32 s27, s33, s27
	s_cmp_eq_u32 s26, 6
	s_cselect_b32 s27, s34, s27
	s_cmp_eq_u32 s26, 7
	s_cselect_b32 s26, s35, s27
	s_and_b32 s27, s41, 0xffffff
	s_add_i32 s13, s26, s27
	v_mov_b32_e32 v34, s20
	s_ashr_i32 s10, s20, 1
	s_ashr_i32 s11, s10, 31
	s_lshl_b64 s[10:11], s[10:11], 10
	v_lshl_add_u64 v[2:3], v[20:21], 0, s[10:11]
	global_load_dwordx4 v[48:51], v[2:3], off
.Lsc_rw1:
	s_cmp_eq_u32 s45, 0
	s_cbranch_scc1 .Lsc_rw2
	v_readfirstlane_b32 s41, v36
	s_nop 0
	s_ashr_i32 s26, s41, 24
	s_cmp_eq_u32 s26, 1
	s_cselect_b32 s27, s6, 0
	s_cmp_eq_u32 s26, 2
	s_cselect_b32 s27, s7, s27
	s_cmp_eq_u32 s26, 3
	s_cselect_b32 s27, s30, s27
	s_cmp_eq_u32 s26, 4
	s_cselect_b32 s27, s31, s27
	s_cmp_eq_u32 s26, 5
	s_cselect_b32 s27, s33, s27
	s_cmp_eq_u32 s26, 6
	s_cselect_b32 s27, s34, s27
	s_cmp_eq_u32 s26, 7
	s_cselect_b32 s26, s35, s27
	s_and_b32 s27, s41, 0xffffff
	s_add_i32 s14, s26, s27
	v_mov_b32_e32 v36, s24
	s_ashr_i32 s10, s24, 1
	s_ashr_i32 s11, s10, 31
	s_lshl_b64 s[10:11], s[10:11], 10
	v_lshl_add_u64 v[2:3], v[20:21], 0, s[10:11]
	global_load_dwordx4 v[52:55], v[2:3], off
.Lsc_rw2:
	s_cmp_eq_u32 s48, 0
	s_cbranch_scc1 .Lsc_rw3
	v_readfirstlane_b32 s41, v38
	s_nop 0
	s_ashr_i32 s26, s41, 24
	s_cmp_eq_u32 s26, 1
	s_cselect_b32 s27, s6, 0
	s_cmp_eq_u32 s26, 2
	s_cselect_b32 s27, s7, s27
	s_cmp_eq_u32 s26, 3
	s_cselect_b32 s27, s30, s27
	s_cmp_eq_u32 s26, 4
	s_cselect_b32 s27, s31, s27
	s_cmp_eq_u32 s26, 5
	s_cselect_b32 s27, s33, s27
	s_cmp_eq_u32 s26, 6
	s_cselect_b32 s27, s34, s27
	s_cmp_eq_u32 s26, 7
	s_cselect_b32 s26, s35, s27
	s_and_b32 s27, s41, 0xffffff
	s_add_i32 s15, s26, s27
	v_mov_b32_e32 v38, s22
	s_ashr_i32 s10, s22, 1
	s_ashr_i32 s11, s10, 31
	s_lshl_b64 s[10:11], s[10:11], 10
	v_lshl_add_u64 v[2:3], v[20:21], 0, s[10:11]
	global_load_dwordx4 v[56:59], v[2:3], off
.Lsc_rw3:
	s_waitcnt vmcnt(0)
	s_mov_b32 s26, s12
	s_mov_b32 s27, 0
	s_lshl_b64 s[10:11], s[26:27], 3
	s_add_u32 s10, s16, s10
	s_addc_u32 s11, s17, s11
	s_lshl_b64 s[28:29], s[26:27], 2
	s_add_u32 s28, s38, s28
	s_addc_u32 s29, s39, s29
	s_lshl_b64 s[26:27], s[26:27], 10
	v_lshl_add_u64 v[2:3], v[22:23], 0, s[26:27]
	s_and_saveexec_b64 s[26:27], s[8:9]
	global_store_dwordx2 v1, v[32:33], s[10:11]
	global_store_dword v1, v40, s[28:29]
	s_or_b64 exec, exec, s[26:27]
	global_store_dwordx4 v[2:3], v[44:47], off
	s_cmp_eq_u32 s44, 0
	s_cbranch_scc1 .Lsc_st1
	s_mov_b32 s26, s13
	s_mov_b32 s27, 0
	s_lshl_b64 s[10:11], s[26:27], 3
	s_add_u32 s10, s16, s10
	s_addc_u32 s11, s17, s11
	s_lshl_b64 s[28:29], s[26:27], 2
	s_add_u32 s28, s38, s28
	s_addc_u32 s29, s39, s29
	s_lshl_b64 s[26:27], s[26:27], 10
	v_lshl_add_u64 v[2:3], v[22:23], 0, s[26:27]
	s_and_saveexec_b64 s[26:27], s[8:9]
	global_store_dwordx2 v1, v[34:35], s[10:11]
	global_store_dword v1, v41, s[28:29]
	s_or_b64 exec, exec, s[26:27]
	global_store_dwordx4 v[2:3], v[48:51], off
.Lsc_st1:
	s_cmp_eq_u32 s45, 0
	s_cbranch_scc1 .Lsc_st2
	s_mov_b32 s26, s14
	s_mov_b32 s27, 0
	s_lshl_b64 s[10:11], s[26:27], 3
	s_add_u32 s10, s16, s10
	s_addc_u32 s11, s17, s11
	s_lshl_b64 s[28:29], s[26:27], 2
	s_add_u32 s28, s38, s28
	s_addc_u32 s29, s39, s29
	s_lshl_b64 s[26:27], s[26:27], 10
	v_lshl_add_u64 v[2:3], v[22:23], 0, s[26:27]
	s_and_saveexec_b64 s[26:27], s[8:9]
	global_store_dwordx2 v1, v[36:37], s[10:11]
	global_store_dword v1, v42, s[28:29]
	s_or_b64 exec, exec, s[26:27]
	global_store_dwordx4 v[2:3], v[52:55], off
.Lsc_st2:
	s_cmp_eq_u32 s48, 0
	s_cbranch_scc1 .Lsc_st3
	s_mov_b32 s26, s15
	s_mov_b32 s27, 0
	s_lshl_b64 s[10:11], s[26:27], 3
	s_add_u32 s10, s16, s10
	s_addc_u32 s11, s17, s11
	s_lshl_b64 s[28:29], s[26:27], 2
	s_add_u32 s28, s38, s28
	s_addc_u32 s29, s39, s29
	s_lshl_b64 s[26:27], s[26:27], 10
	v_lshl_add_u64 v[2:3], v[22:23], 0, s[26:27]
	s_and_saveexec_b64 s[20:21], s[8:9]
	global_store_dwordx2 v1, v[38:39], s[10:11]
	global_store_dword v1, v43, s[28:29]
	s_or_b64 exec, exec, s[20:21]
	global_store_dwordx4 v[2:3], v[56:59], off
.Lsc_st3:
	s_add_i32 s40, s40, s52
	s_add_u32 s18, s18, s62
	s_addc_u32 s19, s19, s63
	s_cmp_lt_i32 s40, 0x10000
	s_cbranch_scc1 .LBB0_1085

.LBB0_1159:
	s_or_b64 exec, exec, s[40:41]
	s_mov_b64 s[4:5], s[0:1]
	s_waitcnt lgkmcnt(0)
	s_barrier
	s_load_dwordx2 s[12:13], s[4:5], 0xd0
	v_readlane_b32 s4, v255, 21
	v_readlane_b32 s5, v255, 22
	s_waitcnt vmcnt(0)
	v_mov_b32_e32 v0, 0x10000
	s_waitcnt lgkmcnt(0)
	s_add_u32 s4, s12, s4
	s_addc_u32 s5, s13, s5
	s_add_u32 s8, s4, 0x10000
	global_load_dword v0, v0, s[4:5] sc1
	s_addc_u32 s9, s5, 0
	global_load_dword v2, v1, s[8:9] offset:256 sc1
	global_load_dword v3, v1, s[8:9] offset:512 sc1
	global_load_dword v4, v1, s[8:9] offset:768 sc1
	global_load_dword v5, v1, s[8:9] offset:1024 sc1
	global_load_dword v7, v1, s[8:9] offset:1280 sc1
	global_load_dword v8, v1, s[8:9] offset:1536 sc1
	global_load_dword v9, v1, s[8:9] offset:1792 sc1
	s_waitcnt vmcnt(7)
	v_readfirstlane_b32 s4, v0
	s_nop 0
	s_addk_i32 s4, 0xff
	s_and_b32 s5, s4, 0xffffff00
	s_waitcnt vmcnt(6)
	v_readfirstlane_b32 s6, v2
	s_nop 0
	s_addk_i32 s6, 0xff
	s_and_b32 s6, s6, 0xffffff00
	s_add_i32 s5, s6, s5
	s_waitcnt vmcnt(5)
	v_readfirstlane_b32 s6, v3
	s_nop 0
	s_addk_i32 s6, 0xff
	s_and_b32 s6, s6, 0xffffff00
	s_add_i32 s6, s6, s5
	s_waitcnt vmcnt(4)
	v_readfirstlane_b32 s7, v4
	s_nop 0
	s_addk_i32 s7, 0xff
	s_and_b32 s7, s7, 0xffffff00
	s_add_i32 s7, s7, s6
	s_waitcnt vmcnt(3)
	v_readfirstlane_b32 s10, v5
	s_nop 0
	s_addk_i32 s10, 0xff
	s_and_b32 s10, s10, 0xffffff00
	s_add_i32 s10, s10, s7
	s_waitcnt vmcnt(2)
	v_readfirstlane_b32 s11, v7
	s_nop 0
	s_addk_i32 s11, 0xff
	s_and_b32 s11, s11, 0xffffff00
	s_add_i32 s11, s11, s10
	s_waitcnt vmcnt(1)
	v_readfirstlane_b32 s14, v8
	s_nop 0
	s_addk_i32 s14, 0xff
	s_and_b32 s15, s14, 0xffffff00
	s_add_i32 s15, s15, s11
	s_waitcnt vmcnt(0)
	v_readfirstlane_b32 s8, v9
	s_nop 0
	s_addk_i32 s8, 0xff
	s_and_b32 s8, s8, 0xffffff00
	s_add_i32 s8, s8, s15
	s_ashr_i32 s33, s8, 8
	v_mbcnt_lo_u32_b32 v0, -1, 0
	v_mbcnt_hi_u32_b32 v0, -1, v0
	s_mul_i32 s38, s33, 28
	v_add_u32_e32 v10, s67, v0
	s_cmp_lt_i32 s76, s38
	v_readfirstlane_b32 s14, v10
	s_cbranch_scc0 .LBB0_1181
	v_readlane_b32 s8, v253, 7
	s_sub_i32 s9, s33, s8
	v_readlane_b32 s8, v253, 8
	s_cmp_gt_i32 s9, 7
	s_mov_b32 s26, s8
	v_readlane_b32 s8, v253, 9
	s_cbranch_scc1 .LBB0_1162
	s_abs_i32 s8, s9
	v_cvt_f32_u32_e32 v0, s8
	s_ashr_i32 s16, s9, 31
	v_readlane_b32 s17, v254, 10
	s_xor_b32 s16, s17, s16
	v_rcp_iflag_f32_e32 v0, v0
	s_sub_i32 s17, 0, s8
	v_readlane_b32 s20, v254, 12
	v_mul_f32_e32 v0, 0x4f7ffffe, v0
	v_cvt_u32_f32_e32 v0, v0
	s_nop 0
	v_readfirstlane_b32 s18, v0
	s_mul_i32 s17, s17, s18
	s_mul_hi_u32 s17, s18, s17
	s_add_i32 s18, s18, s17
	s_mul_hi_u32 s17, s20, s18
	s_mul_i32 s18, s17, s8
	s_sub_i32 s18, s20, s18
	s_add_i32 s19, s17, 1
	s_sub_i32 s20, s18, s8
	s_cmp_ge_u32 s18, s8
	s_cselect_b32 s17, s19, s17
	s_cselect_b32 s18, s20, s18
	s_add_i32 s19, s17, 1
	s_cmp_ge_u32 s18, s8
	s_cselect_b32 s8, s19, s17
	s_xor_b32 s8, s8, s16
	s_sub_i32 s8, s8, s16
	s_mul_i32 s9, s8, s9
	v_readlane_b32 s16, v254, 11
	s_sub_i32 s9, s16, s9
	v_readlane_b32 s16, v253, 7
	s_add_i32 s26, s9, s16

.LBB0_1226:
	s_or_b64 exec, exec, s[40:41]
	s_mov_b64 s[4:5], s[0:1]
	s_waitcnt lgkmcnt(0)
	s_barrier
	s_load_dwordx2 s[8:9], s[4:5], 0xd0
	v_readlane_b32 s4, v255, 21
	v_readlane_b32 s5, v255, 22
	v_mov_b32_e32 v0, 0x10000
	s_waitcnt lgkmcnt(0)
	s_add_u32 s4, s8, s4
	s_addc_u32 s5, s9, s5
	s_add_u32 s6, s4, 0x10000
	global_load_dword v0, v0, s[4:5] sc1
	s_addc_u32 s7, s5, 0
	global_load_dword v2, v1, s[6:7] offset:256 sc1
	global_load_dword v3, v1, s[6:7] offset:512 sc1
	global_load_dword v4, v1, s[6:7] offset:768 sc1
	global_load_dword v5, v1, s[6:7] offset:1024 sc1
	global_load_dword v7, v1, s[6:7] offset:1280 sc1
	global_load_dword v8, v1, s[6:7] offset:1536 sc1
	global_load_dword v9, v1, s[6:7] offset:1792 sc1
	s_waitcnt vmcnt(7)
	v_readfirstlane_b32 s4, v0
	s_nop 0
	s_addk_i32 s4, 0xff
	s_and_b32 s5, s4, 0xffffff00
	s_ashr_i32 s26, s4, 8
	s_waitcnt vmcnt(6)
	v_readfirstlane_b32 s4, v2
	s_nop 0
	s_addk_i32 s4, 0xff
	s_and_b32 s4, s4, 0xffffff00
	s_add_i32 s4, s4, s5
	s_ashr_i32 s27, s4, 8
	s_waitcnt vmcnt(5)
	v_readfirstlane_b32 s5, v3
	s_nop 0
	s_addk_i32 s5, 0xff
	s_and_b32 s5, s5, 0xffffff00
	s_add_i32 s5, s5, s4
	s_ashr_i32 s28, s5, 8
	s_waitcnt vmcnt(4)
	v_readfirstlane_b32 s4, v4
	s_nop 0
	s_addk_i32 s4, 0xff
	s_and_b32 s4, s4, 0xffffff00
	s_add_i32 s4, s4, s5
	s_ashr_i32 s29, s4, 8
	s_waitcnt vmcnt(3)
	v_readfirstlane_b32 s5, v5
	s_nop 0
	s_addk_i32 s5, 0xff
	s_and_b32 s5, s5, 0xffffff00
	s_add_i32 s5, s5, s4
	s_ashr_i32 s30, s5, 8
	s_waitcnt vmcnt(2)
	v_readfirstlane_b32 s4, v7
	s_nop 0
	s_addk_i32 s4, 0xff
	s_and_b32 s4, s4, 0xffffff00
	s_add_i32 s4, s4, s5
	s_ashr_i32 s31, s4, 8
	s_waitcnt vmcnt(1)
	v_readfirstlane_b32 s5, v8
	s_nop 0
	s_addk_i32 s5, 0xff
	s_and_b32 s5, s5, 0xffffff00
	s_add_i32 s5, s5, s4
	s_ashr_i32 s33, s5, 8
	s_waitcnt vmcnt(0)
	v_readfirstlane_b32 s4, v9
	s_nop 0
	s_addk_i32 s4, 0xff
	s_and_b32 s37, s4, 0xffffff00
	s_add_i32 s37, s37, s5
	s_ashr_i32 s34, s37, 8
	s_add_u32 s35, s8, 0x18800000
	s_addc_u32 s36, s9, 0
	s_add_u32 s6, s8, 0x3ae00000
	s_addc_u32 s7, s9, 0
	s_add_u32 s10, s8, 0x200000
	s_addc_u32 s11, s9, 0
	v_readlane_b32 s4, v255, 23
	s_add_u32 s12, s8, 0x5c00000
	v_readlane_b32 s5, v255, 24
	s_addc_u32 s13, s9, 0
	s_mov_b64 s[8:9], -1
	s_and_b64 vcc, exec, s[4:5]
	s_cbranch_vccz .LBB0_1272
	v_mbcnt_lo_u32_b32 v0, -1, 0
	v_mbcnt_hi_u32_b32 v0, -1, v0
	s_ashr_i32 s38, s37, 6
	v_add_u32_e32 v0, s67, v0
	s_cmp_lt_i32 s76, s38
	s_cselect_b64 s[8:9], -1, 0
	v_readfirstlane_b32 s4, v0
	s_cmp_ge_i32 s76, s38
	s_cbranch_scc1 .LBB0_1231
	v_readlane_b32 s5, v253, 12
	s_sub_i32 s14, s34, s5
	s_cmp_gt_i32 s14, 7
	v_readlane_b32 s63, v253, 13
	v_readlane_b32 s5, v253, 14
	s_cbranch_scc1 .LBB0_1230
	s_abs_i32 s5, s14
	v_cvt_f32_u32_e32 v2, s5
	s_sub_i32 s16, 0, s5
	v_readlane_b32 s20, v253, 10
	s_ashr_i32 s15, s14, 31
	v_rcp_iflag_f32_e32 v2, v2
	s_nop 0
	v_mul_f32_e32 v2, 0x4f7ffffe, v2
	v_cvt_u32_f32_e32 v2, v2
	s_nop 0
	v_readfirstlane_b32 s17, v2
	s_mul_i32 s16, s16, s17
	s_mul_hi_u32 s16, s17, s16
	s_add_i32 s17, s17, s16
	s_mul_hi_u32 s16, s20, s17
	s_mul_i32 s17, s16, s5
	s_sub_i32 s17, s20, s17
	s_add_i32 s18, s16, 1
	s_sub_i32 s19, s17, s5
	s_cmp_ge_u32 s17, s5
	s_cselect_b32 s16, s18, s16
	s_cselect_b32 s17, s19, s17
	s_add_i32 s18, s16, 1
	s_cmp_ge_u32 s17, s5
	s_cselect_b32 s5, s18, s16
	s_xor_b32 s5, s5, s15
	s_sub_i32 s5, s5, s15
	s_mul_i32 s14, s5, s14
	s_sub_i32 s14, s20, s14
	v_readlane_b32 s15, v253, 12
	s_add_i32 s63, s14, s15
